# ssm_post token loop: loop-invariant parameter loads (4 dwords + 4 dwordx4 per token) done once before the loop; gate row loads issued at the top of the iteration instead of behind two full waits
# speedup vs baseline: 1.0020x; 1.0020x over previous
; __device__ void phase_ssm_post(KParams& p, int bid, int nb, char* smem) {
;     ...
;   for (int t = bid * 4 + w; t < T; t += nb * 4) {
;     float y[4][4];
;     float ss0 = 0.f, ss1 = 0.f;
; #pragma unroll
;     for (int c = 0; c < 4; ++c) {
;       const int c0 = c * 256 + lane * 4;
;       const int h = c0 >> 6;
;       const float dsk = p.d_skip_f[h] + p.d_skip_b[h];
;     ...
;       const float4 nw = *reinterpret_cast<const float4*>(p.ssm_norm_w + c0);
.Lgb_wd_6:
.LBB0_1000:
	s_or_b64 exec, exec, s[6:7]
	s_movk_i32 s6, 0x2000
	v_mov_b32_e32 v191, 0
	s_mov_b64 s[16:17], s[0:1]
	v_cmp_gt_i32_e64 s[6:7], s6, v186
	v_lshlrev_b32_e32 v134, 2, v190
	s_waitcnt lgkmcnt(0)
	s_barrier
	s_and_saveexec_b64 s[18:19], s[6:7]
	s_cbranch_execz .LBB0_1005
	v_cmp_lt_i32_e32 vcc, v179, v180
	s_load_dwordx4 s[12:15], s[16:17], 0x90
	s_load_dwordx2 s[22:23], s[16:17], 0xa0
	v_cndmask_b32_e32 v2, v178, v179, vcc
	v_cmp_lt_i32_e32 vcc, v181, v180
	s_load_dwordx4 s[24:27], s[16:17], 0x208
	s_load_dwordx2 s[28:29], s[16:17], 0x228
	s_load_dwordx2 s[30:31], s[16:17], 0x1f0
	s_load_dwordx2 s[36:37], s[16:17], 0x1a8
	s_load_dwordx2 s[38:39], s[16:17], 0x118
	s_load_dwordx2 s[40:41], s[16:17], 0x128
	v_lshlrev_b32_e32 v39, 2, v2
	v_cndmask_b32_e32 v2, v178, v181, vcc
	v_or_b32_e32 v6, 0x100, v190
	v_or_b32_e32 v10, 0x200, v190
	v_or_b32_e32 v14, 0x300, v190
	v_lshlrev_b32_e32 v74, 2, v2
	v_lshrrev_b32_e32 v2, 2, v184
	v_lshrrev_b32_e32 v6, 4, v6
	v_lshrrev_b32_e32 v10, 4, v10
	v_lshrrev_b32_e32 v14, 4, v14
	s_lshl_b32 s20, s34, 2
	v_and_b32_e32 v4, 12, v2
	v_mov_b32_e32 v5, v191
	v_and_b32_e32 v8, 28, v6
	v_mov_b32_e32 v9, v191
	v_and_b32_e32 v12, 44, v10
	v_mov_b32_e32 v13, v191
	v_and_b32_e32 v16, 60, v14
	v_mov_b32_e32 v17, v191
	s_waitcnt lgkmcnt(0)
	v_lshl_add_u64 v[2:3], s[12:13], 0, v[4:5]
	v_lshl_add_u64 v[6:7], s[12:13], 0, v[8:9]
	v_lshl_add_u64 v[10:11], s[12:13], 0, v[12:13]
	v_lshl_add_u64 v[14:15], s[12:13], 0, v[16:17]
	v_mov_b32_e32 v135, v191
	v_lshlrev_b32_e32 v24, 1, v190
	v_mov_b32_e32 v25, v191
	s_ashr_i32 s21, s20, 31
	v_lshlrev_b64 v[34:35], 12, v[186:187]
	s_movk_i32 s12, 0xc00
	v_mov_b64_e32 v[36:37], s[30:31]
	v_lshl_add_u64 v[4:5], s[14:15], 0, v[4:5]
	v_lshl_add_u64 v[8:9], s[14:15], 0, v[8:9]
	v_lshl_add_u64 v[12:13], s[14:15], 0, v[12:13]
	v_lshl_add_u64 v[16:17], s[14:15], 0, v[16:17]
	v_lshl_add_u64 v[18:19], s[22:23], 0, v[134:135]
	v_lshl_add_u64 v[20:21], s[24:25], 0, v[24:25]
	v_lshl_add_u64 v[22:23], s[26:27], 0, v[24:25]
	v_lshl_add_u64 v[24:25], s[36:37], 0, v[24:25]
	v_lshl_add_u64 v[26:27], s[38:39], 0, v[190:191]
	v_lshl_add_u64 v[28:29], v[186:187], 2, s[40:41]
	s_lshl_b64 s[14:15], s[20:21], 2
	v_lshlrev_b64 v[30:31], 11, v[186:187]
	s_lshl_b64 s[22:23], s[20:21], 11
	v_lshlrev_b32_e32 v32, 3, v184
	v_mov_b32_e32 v33, v191
	v_lshl_add_u64 v[34:35], s[28:29], 0, v[34:35]
	s_lshl_b64 s[24:25], s[20:21], 12
	v_mad_i64_i32 v[36:37], s[12:13], v186, s12, v[36:37]
	s_mul_i32 s26, s34, 0x3000
	s_mul_hi_i32 s27, s20, 0xc00
	s_mov_b64 s[28:29], 0
	s_mov_b32 s30, 0x3b000000
	v_mov_b32_e32 v38, 0x358637bd
	s_mov_b32 s21, 0x800000
	s_mov_b32 s31, 0x42fe0000
	s_mov_b32 s36, 0xc0c0500
	s_mov_b32 s37, 0x40c0c00
	s_movk_i32 s38, 0x1fff
	v_mov_b32_e32 v75, v186
	global_load_dword v100, v[10:11], off
	global_load_dword v101, v[12:13], off
	global_load_dword v102, v[14:15], off
	global_load_dword v103, v[16:17], off
	global_load_dwordx4 v[104:107], v[18:19], off
	global_load_dwordx4 v[108:111], v[18:19], off offset:1024
	global_load_dwordx4 v[112:115], v[18:19], off offset:2048
	global_load_dwordx4 v[116:119], v[18:19], off offset:3072
	s_waitcnt vmcnt(0)
	s_branch .LBB0_1003

; __device__ __forceinline__ float bflo(uint32_t w) { return __uint_as_float(w << 16); }
; __device__ __forceinline__ float bfhi(uint32_t w) { return __uint_as_float(w & 0xffff0000u); }
; __device__ __forceinline__ float silu_f(float v) { return v / (1.f + __expf(-v)); }
; __device__ void phase_ssm_post(KParams& p, int bid, int nb, char* smem) {
;     ...
;   for (int t = bid * 4 + w; t < T; t += nb * 4) {
;     float y[4][4];
;     float ss0 = 0.f, ss1 = 0.f;
; #pragma unroll
;     for (int c = 0; c < 4; ++c) {
;       const int c0 = c * 256 + lane * 4;
;       const int h = c0 >> 6;
;       const float dsk = p.d_skip_f[h] + p.d_skip_b[h];
;       const uint2 aq = *reinterpret_cast<const uint2*>(reinterpret_cast<const bf16_t*>(p.yf) + (size_t)t * 1024 + c0);
;       const uint2 bb = *reinterpret_cast<const uint2*>(reinterpret_cast<const bf16_t*>(p.yb) + (size_t)t * 1024 + c0);
;       const float4 a = float4{bflo(aq.x), bfhi(aq.x), bflo(aq.y), bfhi(aq.y)};
;       const float4 bq = float4{bflo(bb.x), bfhi(bb.x), bflo(bb.y), bfhi(bb.y)};
;       const uint2 xq = *reinterpret_cast<const uint2*>(p.act_tm + (size_t)t * DXBC + c0);
;       const uint2 zz = *reinterpret_cast<const uint2*>(p.z + (size_t)t * 1024 + c0);
;       y[c][0] = (a.x + bq.x + dsk * bflo(xq.x)) * silu_f(bflo(zz.x));
;       y[c][1] = (a.y + bq.y + dsk * bfhi(xq.x)) * silu_f(bfhi(zz.x));
;       y[c][2] = (a.z + bq.z + dsk * bflo(xq.y)) * silu_f(bflo(zz.y));
;       y[c][3] = (a.w + bq.w + dsk * bfhi(xq.y)) * silu_f(bfhi(zz.y));
;       const float q = y[c][0] * y[c][0] + y[c][1] * y[c][1] + y[c][2] * y[c][2] + y[c][3] * y[c][3];
;       if (c < 2) ss0 += q; else ss1 += q;
;     }
.LBB0_1003:
	v_lshl_add_u64 v[58:59], v[20:21], 0, v[30:31]
	v_lshl_add_u64 v[68:69], v[22:23], 0, v[30:31]
	global_load_dword v40, v[2:3], off
	global_load_dword v42, v[4:5], off
	v_lshl_add_u64 v[56:57], v[24:25], 0, v[30:31]
	global_load_dword v41, v[6:7], off
	global_load_dword v43, v[8:9], off
	global_load_dwordx2 v[54:55], v[56:57], off offset:512
	global_load_dwordx2 v[44:45], v[56:57], off
	global_load_dwordx2 v[66:67], v[58:59], off offset:512
	global_load_dwordx2 v[64:65], v[58:59], off
	global_load_dwordx2 v[62:63], v[68:69], off offset:512
	global_load_dwordx2 v[60:61], v[68:69], off
	v_lshl_add_u64 v[70:71], v[36:37], 0, v[32:33]
	global_load_dwordx2 v[50:51], v[70:71], off offset:512
	global_load_dwordx2 v[46:47], v[70:71], off
	global_load_dwordx2 v[76:77], v[56:57], off offset:1024
	global_load_dwordx2 v[78:79], v[56:57], off offset:1536
	global_load_dwordx2 v[72:73], v[58:59], off offset:1024
	global_load_dwordx2 v[80:81], v[58:59], off offset:1536
	global_load_dwordx2 v[82:83], v[68:69], off offset:1024
	global_load_dwordx2 v[84:85], v[68:69], off offset:1536
	global_load_dwordx2 v[48:49], v[70:71], off offset:1024
	global_load_dwordx2 v[52:53], v[70:71], off offset:1536
	v_lshl_add_u64 v[128:129], v[34:35], 0, v[32:33]
	global_load_dwordx2 v[120:121], v[128:129], off
	global_load_dwordx2 v[122:123], v[128:129], off offset:512
	global_load_dwordx2 v[124:125], v[128:129], off offset:1024
	global_load_dwordx2 v[126:127], v[128:129], off offset:1536
	s_waitcnt vmcnt(13)
	v_and_b32_e32 v69, 0xffff0000, v50
	s_waitcnt vmcnt(12)
	v_and_b32_e32 v68, 0xffff0000, v46
	v_pk_add_f32 v[56:57], v[40:41], v[42:43]
	v_lshlrev_b32_e32 v71, 16, v54
	v_lshlrev_b32_e32 v87, 16, v44
	v_lshlrev_b32_e32 v41, 16, v66
	v_lshlrev_b32_e32 v40, 16, v64
	v_lshlrev_b32_e32 v59, 16, v62
	v_lshlrev_b32_e32 v58, 16, v60
	v_and_b32_e32 v42, 0xffff0000, v64
	v_and_b32_e32 v64, 0xffff0000, v60
	v_lshlrev_b32_e32 v60, 16, v46
	v_mul_f32_e32 v46, 0xbfb8aa3b, v87
	v_pk_add_f32 v[40:41], v[40:41], v[58:59]
	v_mul_f32_e32 v59, 0xbfb8aa3b, v71
	v_and_b32_e32 v88, 0xffff0000, v54
	v_and_b32_e32 v89, 0xffff0000, v44
	v_and_b32_e32 v43, 0xffff0000, v66
	v_lshlrev_b32_e32 v44, 16, v65
	v_and_b32_e32 v54, 0xffff0000, v65
	v_and_b32_e32 v65, 0xffff0000, v62
	v_exp_f32_e32 v58, v46
	v_exp_f32_e32 v59, v59
	v_lshlrev_b32_e32 v66, 16, v61
	v_and_b32_e32 v62, 0xffff0000, v61
	v_lshlrev_b32_e32 v61, 16, v50
	v_mul_f32_e32 v50, 0xbfb8aa3b, v89
	v_pk_add_f32 v[42:43], v[42:43], v[64:65]
	v_mul_f32_e32 v65, 0xbfb8aa3b, v88
	v_exp_f32_e32 v64, v50
	v_exp_f32_e32 v65, v65
	v_pk_add_f32 v[58:59], v[58:59], 1.0 op_sel_hi:[1,0]
	v_pk_fma_f32 v[40:41], v[56:57], v[60:61], v[40:41]
	v_div_scale_f32 v46, s[12:13], v59, v59, v71
	v_pk_fma_f32 v[42:43], v[56:57], v[68:69], v[42:43]
	v_pk_add_f32 v[60:61], v[64:65], 1.0 op_sel_hi:[1,0]
	v_div_scale_f32 v64, s[12:13], v58, v58, v87
	v_rcp_f32_e32 v68, v46
	v_rcp_f32_e32 v69, v64
	v_div_scale_f32 v50, vcc, v71, v59, v71
	v_fma_f32 v96, -v46, v68, 1.0
	v_fma_f32 v97, -v64, v69, 1.0
	v_fmac_f32_e32 v68, v96, v68
	v_div_scale_f32 v65, s[12:13], v87, v58, v87
	v_fmac_f32_e32 v69, v97, v69
	v_mul_f32_e32 v96, v50, v68
	v_div_scale_f32 v94, s[40:41], v61, v61, v88
	v_mul_f32_e32 v97, v65, v69
	v_fma_f32 v98, -v46, v96, v50
	v_rcp_f32_e32 v95, v94
	v_fma_f32 v99, -v64, v97, v65
	v_fmac_f32_e32 v96, v98, v68
	v_fmac_f32_e32 v97, v99, v69
	v_fma_f32 v46, -v46, v96, v50
	v_fma_f32 v50, -v64, v97, v65
	v_div_fmas_f32 v46, v46, v68, v96
	s_mov_b64 vcc, s[12:13]
	v_div_fixup_f32 v59, v46, v59, v71
	v_div_fmas_f32 v46, v50, v69, v97
	v_div_fixup_f32 v58, v46, v58, v87
	v_fma_f32 v46, -v94, v95, 1.0
	v_fmac_f32_e32 v95, v46, v95
	v_div_scale_f32 v46, vcc, v88, v61, v88
	v_mul_f32_e32 v50, v46, v95
	v_pk_mul_f32 v[40:41], v[40:41], v[58:59]
	v_fma_f32 v58, -v94, v50, v46
	v_fmac_f32_e32 v50, v58, v95
	v_div_scale_f32 v58, s[12:13], v60, v60, v89
	v_rcp_f32_e32 v64, v58
	v_fma_f32 v46, -v94, v50, v46
	v_div_fmas_f32 v46, v46, v95, v50
	v_div_fixup_f32 v59, v46, v61, v88
	v_fma_f32 v46, -v58, v64, 1.0
	v_fmac_f32_e32 v64, v46, v64
	v_div_scale_f32 v46, vcc, v89, v60, v89
	v_mul_f32_e32 v50, v46, v64
	v_fma_f32 v61, -v58, v50, v46
	v_fmac_f32_e32 v50, v61, v64
	v_lshlrev_b32_e32 v90, 16, v55
	v_lshlrev_b32_e32 v91, 16, v45
	v_fma_f32 v46, -v58, v50, v46
	v_mul_f32_e32 v70, 0xbfb8aa3b, v91
	v_div_fmas_f32 v46, v46, v64, v50
	v_mul_f32_e32 v50, 0xbfb8aa3b, v90
	v_exp_f32_e32 v70, v70
	v_exp_f32_e32 v71, v50
	v_div_fixup_f32 v58, v46, v60, v89
	v_pk_mul_f32 v[42:43], v[42:43], v[58:59]
	v_and_b32_e32 v92, 0xffff0000, v55
	v_pk_add_f32 v[58:59], v[70:71], 1.0 op_sel_hi:[1,0]
	v_and_b32_e32 v93, 0xffff0000, v45
	v_div_scale_f32 v46, s[12:13], v59, v59, v90
	v_rcp_f32_e32 v50, v46
	v_lshlrev_b32_e32 v45, 16, v67
	v_and_b32_e32 v55, 0xffff0000, v67
	v_lshlrev_b32_e32 v67, 16, v63
	v_pk_add_f32 v[44:45], v[44:45], v[66:67]
	v_lshlrev_b32_e32 v61, 16, v51
	v_lshlrev_b32_e32 v60, 16, v47
	v_pk_fma_f32 v[44:45], v[56:57], v[60:61], v[44:45]
	v_fma_f32 v60, -v46, v50, 1.0
	v_fmac_f32_e32 v50, v60, v50
	v_mov_b32_e32 v60, v100
	v_mov_b32_e32 v64, v101
	v_mov_b32_e32 v61, v102
	v_mov_b32_e32 v65, v103
	v_div_scale_f32 v66, vcc, v90, v59, v90
	v_mul_f32_e32 v67, v66, v50
	v_fma_f32 v68, -v46, v67, v66
	v_fmac_f32_e32 v67, v68, v50
	v_fma_f32 v46, -v46, v67, v66
	v_div_scale_f32 v66, s[12:13], v58, v58, v91
	v_rcp_f32_e32 v68, v66
	v_div_fmas_f32 v46, v46, v50, v67
	v_div_fixup_f32 v59, v46, v59, v90
	v_mul_f32_e32 v86, 0xbfb8aa3b, v93
	v_fma_f32 v46, -v66, v68, 1.0
	v_fmac_f32_e32 v68, v46, v68
	v_div_scale_f32 v46, vcc, v91, v58, v91
	v_mul_f32_e32 v50, v46, v68
	v_fma_f32 v67, -v66, v50, v46
	v_fmac_f32_e32 v50, v67, v68
	v_fma_f32 v46, -v66, v50, v46
	v_div_fmas_f32 v46, v46, v68, v50
	v_mul_f32_e32 v50, 0xbfb8aa3b, v92
	v_exp_f32_e32 v86, v86
	v_exp_f32_e32 v87, v50
	v_div_fixup_f32 v58, v46, v58, v91
	v_and_b32_e32 v63, 0xffff0000, v63
	v_pk_mul_f32 v[44:45], v[44:45], v[58:59]
	v_pk_add_f32 v[58:59], v[86:87], 1.0 op_sel_hi:[1,0]
	v_pk_add_f32 v[54:55], v[54:55], v[62:63]
	v_div_scale_f32 v62, s[12:13], v59, v59, v92
	v_rcp_f32_e32 v63, v62
	v_and_b32_e32 v51, 0xffff0000, v51
	v_and_b32_e32 v50, 0xffff0000, v47
	v_pk_fma_f32 v[46:47], v[56:57], v[50:51], v[54:55]
	v_fma_f32 v50, -v62, v63, 1.0
	v_fmac_f32_e32 v63, v50, v63
	v_div_scale_f32 v50, vcc, v92, v59, v92
	v_mul_f32_e32 v51, v50, v63
	v_fma_f32 v54, -v62, v51, v50
	v_fmac_f32_e32 v51, v54, v63
	v_div_scale_f32 v54, s[12:13], v58, v58, v93
	v_rcp_f32_e32 v55, v54
	v_fma_f32 v50, -v62, v51, v50
	v_div_fmas_f32 v50, v50, v63, v51
	v_div_fixup_f32 v51, v50, v59, v92
	v_fma_f32 v50, -v54, v55, 1.0
	v_fmac_f32_e32 v55, v50, v55
	v_div_scale_f32 v50, vcc, v93, v58, v93
	v_mul_f32_e32 v56, v50, v55
	v_fma_f32 v57, -v54, v56, v50
	v_fmac_f32_e32 v56, v57, v55
	v_fma_f32 v50, -v54, v56, v50
	v_div_fmas_f32 v50, v50, v55, v56
	v_div_fixup_f32 v50, v50, v58, v93
	v_pk_mul_f32 v[46:47], v[46:47], v[50:51]
	v_pk_mul_f32 v[50:51], v[42:43], v[42:43]
	s_waitcnt vmcnt(11)
; __device__ __forceinline__ float bflo(uint32_t w) { return __uint_as_float(w << 16); }
; __device__ __forceinline__ float bfhi(uint32_t w) { return __uint_as_float(w & 0xffff0000u); }
; __device__ __forceinline__ float silu_f(float v) { return v / (1.f + __expf(-v)); }
; __device__ void phase_ssm_post(KParams& p, int bid, int nb, char* smem) {
;     ...
;     for (int c = 0; c < 4; ++c) {
;       const int c0 = c * 256 + lane * 4;
;       const int h = c0 >> 6;
;       const float dsk = p.d_skip_f[h] + p.d_skip_b[h];
;       const uint2 aq = *reinterpret_cast<const uint2*>(reinterpret_cast<const bf16_t*>(p.yf) + (size_t)t * 1024 + c0);
;       const uint2 bb = *reinterpret_cast<const uint2*>(reinterpret_cast<const bf16_t*>(p.yb) + (size_t)t * 1024 + c0);
;       const float4 a = float4{bflo(aq.x), bfhi(aq.x), bflo(aq.y), bfhi(aq.y)};
;       const float4 bq = float4{bflo(bb.x), bfhi(bb.x), bflo(bb.y), bfhi(bb.y)};
;       const uint2 xq = *reinterpret_cast<const uint2*>(p.act_tm + (size_t)t * DXBC + c0);
;       const uint2 zz = *reinterpret_cast<const uint2*>(p.z + (size_t)t * 1024 + c0);
;       y[c][0] = (a.x + bq.x + dsk * bflo(xq.x)) * silu_f(bflo(zz.x));
;       y[c][1] = (a.y + bq.y + dsk * bfhi(xq.x)) * silu_f(bfhi(zz.x));
;       y[c][2] = (a.z + bq.z + dsk * bflo(xq.y)) * silu_f(bflo(zz.y));
;       y[c][3] = (a.w + bq.w + dsk * bfhi(xq.y)) * silu_f(bfhi(zz.y));
;       const float q = y[c][0] * y[c][0] + y[c][1] * y[c][1] + y[c][2] * y[c][2] + y[c][3] * y[c][3];
;       if (c < 2) ss0 += q; else ss1 += q;
;     }
;     ss0 = wave_sum_fast(ss0); ss1 = wave_sum_fast(ss1);
	v_and_b32_e32 v86, 0xffff0000, v76
	v_pk_fma_f32 v[50:51], v[40:41], v[40:41], v[50:51]
	v_lshlrev_b32_e32 v88, 16, v77
	v_pk_fma_f32 v[50:51], v[44:45], v[44:45], v[50:51]
	v_and_b32_e32 v90, 0xffff0000, v77
	v_pk_fma_f32 v[54:55], v[46:47], v[46:47], v[50:51]
	v_mul_f32_e32 v51, 0xbfb8aa3b, v86
	v_exp_f32_e32 v56, v51
	v_mul_f32_e32 v51, 0xbfb8aa3b, v88
	s_waitcnt vmcnt(10)
	v_lshlrev_b32_e32 v57, 16, v78
	v_lshlrev_b32_e32 v59, 16, v76
	v_exp_f32_e32 v58, v51
	v_mul_f32_e32 v51, 0xbfb8aa3b, v90
	v_mul_f32_e32 v50, 0xbfb8aa3b, v59
	v_exp_f32_e32 v62, v51
	v_mul_f32_e32 v51, 0xbfb8aa3b, v57
	v_exp_f32_e32 v50, v50
	v_exp_f32_e32 v51, v51
	s_waitcnt vmcnt(9)
	v_and_b32_e32 v66, 0xffff0000, v72
	s_waitcnt vmcnt(0)
	v_pk_add_f32 v[60:61], v[60:61], v[64:65]
	v_lshlrev_b32_e32 v64, 16, v72
	v_pk_add_f32 v[50:51], v[50:51], 1.0 op_sel_hi:[1,0]
	v_lshlrev_b32_e32 v72, 16, v82
	v_and_b32_e32 v76, 0xffff0000, v82
	v_div_scale_f32 v82, s[12:13], v51, v51, v57
	v_and_b32_e32 v63, 0xffff0000, v78
	v_lshlrev_b32_e32 v65, 16, v80
	v_and_b32_e32 v67, 0xffff0000, v80
	v_lshlrev_b32_e32 v78, 16, v83
	v_and_b32_e32 v80, 0xffff0000, v83
	v_rcp_f32_e32 v83, v82
	v_lshlrev_b32_e32 v68, 16, v73
	v_and_b32_e32 v70, 0xffff0000, v73
	v_lshlrev_b32_e32 v73, 16, v84
	v_pk_add_f32 v[64:65], v[64:65], v[72:73]
	v_lshlrev_b32_e32 v73, 16, v52
	v_lshlrev_b32_e32 v72, 16, v48
	v_pk_fma_f32 v[64:65], v[60:61], v[72:73], v[64:65]
	v_fma_f32 v72, -v82, v83, 1.0
	v_fmac_f32_e32 v83, v72, v83
	v_div_scale_f32 v72, vcc, v57, v51, v57
	v_mul_f32_e32 v73, v72, v83
	v_and_b32_e32 v77, 0xffff0000, v84
	v_fma_f32 v84, -v82, v73, v72
	v_fmac_f32_e32 v73, v84, v83
	v_fma_f32 v72, -v82, v73, v72
	v_div_scale_f32 v82, s[12:13], v50, v50, v59
	v_rcp_f32_e32 v84, v82
	v_div_fmas_f32 v72, v72, v83, v73
	v_div_fixup_f32 v51, v72, v51, v57
	v_lshlrev_b32_e32 v87, 16, v79
	v_fma_f32 v57, -v82, v84, 1.0
	v_fmac_f32_e32 v84, v57, v84
	v_div_scale_f32 v57, vcc, v59, v50, v59
	v_mul_f32_e32 v72, v57, v84
	v_fma_f32 v73, -v82, v72, v57
	v_fmac_f32_e32 v72, v73, v84
	v_fma_f32 v57, -v82, v72, v57
	v_div_fmas_f32 v72, v57, v84, v72
	v_mul_f32_e32 v57, 0xbfb8aa3b, v63
	v_exp_f32_e32 v57, v57
	v_div_fixup_f32 v50, v72, v50, v59
	v_pk_mul_f32 v[50:51], v[64:65], v[50:51]
	v_pk_add_f32 v[64:65], v[66:67], v[76:77]
	v_pk_add_f32 v[56:57], v[56:57], 1.0 op_sel_hi:[1,0]
	v_and_b32_e32 v66, 0xffff0000, v48
	v_div_scale_f32 v59, s[12:13], v57, v57, v63
	v_rcp_f32_e32 v72, v59
	v_and_b32_e32 v67, 0xffff0000, v52
	v_pk_fma_f32 v[64:65], v[60:61], v[66:67], v[64:65]
	v_and_b32_e32 v89, 0xffff0000, v79
	v_fma_f32 v48, -v59, v72, 1.0
	v_fmac_f32_e32 v72, v48, v72
	v_div_scale_f32 v48, vcc, v63, v57, v63
	v_mul_f32_e32 v52, v48, v72
	v_fma_f32 v66, -v59, v52, v48
	v_fmac_f32_e32 v52, v66, v72
	v_fma_f32 v48, -v59, v52, v48
	v_div_scale_f32 v59, s[12:13], v56, v56, v86
	v_rcp_f32_e32 v66, v59
	v_div_fmas_f32 v48, v48, v72, v52
	v_div_fixup_f32 v57, v48, v57, v63
	v_lshlrev_b32_e32 v69, 16, v81
	v_fma_f32 v48, -v59, v66, 1.0
	v_fmac_f32_e32 v66, v48, v66
	v_div_scale_f32 v48, vcc, v86, v56, v86
	v_mul_f32_e32 v52, v48, v66
	v_fma_f32 v63, -v59, v52, v48
	v_fmac_f32_e32 v52, v63, v66
	v_fma_f32 v48, -v59, v52, v48
	v_div_fmas_f32 v48, v48, v66, v52
	v_mul_f32_e32 v52, 0xbfb8aa3b, v87
	v_exp_f32_e32 v59, v52
	v_div_fixup_f32 v56, v48, v56, v86
	v_lshlrev_b32_e32 v79, 16, v85
	v_pk_mul_f32 v[56:57], v[64:65], v[56:57]
	v_pk_add_f32 v[58:59], v[58:59], 1.0 op_sel_hi:[1,0]
	v_pk_add_f32 v[64:65], v[68:69], v[78:79]
	v_div_scale_f32 v48, s[12:13], v59, v59, v87
	v_rcp_f32_e32 v52, v48
	v_lshlrev_b32_e32 v67, 16, v53
	v_lshlrev_b32_e32 v66, 16, v49
	v_pk_fma_f32 v[64:65], v[60:61], v[66:67], v[64:65]
	v_fma_f32 v63, -v48, v52, 1.0
	v_fmac_f32_e32 v52, v63, v52
	v_div_scale_f32 v63, vcc, v87, v59, v87
	v_mul_f32_e32 v66, v63, v52
	v_fma_f32 v67, -v48, v66, v63
	v_fmac_f32_e32 v66, v67, v52
	v_fma_f32 v48, -v48, v66, v63
	v_div_scale_f32 v63, s[12:13], v58, v58, v88
	v_rcp_f32_e32 v67, v63
	v_div_fmas_f32 v48, v48, v52, v66
	v_div_fixup_f32 v59, v48, v59, v87
	v_and_b32_e32 v71, 0xffff0000, v81
	v_fma_f32 v48, -v63, v67, 1.0
	v_fmac_f32_e32 v67, v48, v67
	v_div_scale_f32 v48, vcc, v88, v58, v88
	v_mul_f32_e32 v52, v48, v67
	v_fma_f32 v66, -v63, v52, v48
	v_fmac_f32_e32 v52, v66, v67
	v_fma_f32 v48, -v63, v52, v48
	v_div_fmas_f32 v48, v48, v67, v52
	v_mul_f32_e32 v52, 0xbfb8aa3b, v89
	v_exp_f32_e32 v63, v52
	v_and_b32_e32 v81, 0xffff0000, v85
	v_div_fixup_f32 v58, v48, v58, v88
	v_pk_mul_f32 v[58:59], v[64:65], v[58:59]
	v_pk_add_f32 v[66:67], v[62:63], 1.0 op_sel_hi:[1,0]
	v_pk_add_f32 v[64:65], v[70:71], v[80:81]
	v_div_scale_f32 v62, s[12:13], v67, v67, v89
	v_rcp_f32_e32 v70, v62
	v_and_b32_e32 v53, 0xffff0000, v53
	v_and_b32_e32 v52, 0xffff0000, v49
	v_pk_fma_f32 v[48:49], v[60:61], v[52:53], v[64:65]
	v_fma_f32 v52, -v62, v70, 1.0
	v_fmac_f32_e32 v70, v52, v70
	v_div_scale_f32 v52, vcc, v89, v67, v89
	v_mul_f32_e32 v53, v52, v70
	v_div_scale_f32 v64, s[12:13], v66, v66, v90
	v_fma_f32 v60, -v62, v53, v52
	v_rcp_f32_e32 v65, v64
	v_fmac_f32_e32 v53, v60, v70
	v_fma_f32 v52, -v62, v53, v52
	v_div_fmas_f32 v52, v52, v70, v53
	v_div_fixup_f32 v53, v52, v67, v89
	v_fma_f32 v52, -v64, v65, 1.0
	v_fmac_f32_e32 v65, v52, v65
	v_div_scale_f32 v52, vcc, v90, v66, v90
	v_mul_f32_e32 v67, v52, v65
	v_fma_f32 v70, -v64, v67, v52
	v_fmac_f32_e32 v67, v70, v65
	v_fma_f32 v52, -v64, v67, v52
	v_div_fmas_f32 v52, v52, v65, v67
	v_div_fixup_f32 v52, v52, v66, v90
	v_pk_mul_f32 v[48:49], v[48:49], v[52:53]
	v_pk_mul_f32 v[52:53], v[56:57], v[56:57]
	v_mov_b32_e32 v71, v54
	v_pk_fma_f32 v[52:53], v[50:51], v[50:51], v[52:53]
; __device__ __forceinline__ float bflo(uint32_t w) { return __uint_as_float(w << 16); }
; __device__ __forceinline__ float bfhi(uint32_t w) { return __uint_as_float(w & 0xffff0000u); }
; __device__ void phase_ssm_post(KParams& p, int bid, int nb, char* smem) {
;     ...
;     ss0 = wave_sum_fast(ss0); ss1 = wave_sum_fast(ss1);
;     const float r0 = rsqrtf(ss0 * (1.f / 512.f) + EPS), r1 = rsqrtf(ss1 * (1.f / 512.f) + EPS);
;     uint2 fq[4];
;     float am = 0.f;
; #pragma unroll
;     for (int c = 0; c < 4; ++c) {
;       const int c0 = c * 256 + lane * 4;
;       fq[c] = *reinterpret_cast<const uint2*>(p.ycat + (size_t)t * D + c0);
;       am = fmaxf(am, fmaxf(fmaxf(fabsf(bflo(fq[c].x)), fabsf(bfhi(fq[c].x))), fmaxf(fabsf(bflo(fq[c].y)), fabsf(bfhi(fq[c].y)))));
;       const float rstd = (c < 2) ? r0 : r1;
;       const float4 nw = *reinterpret_cast<const float4*>(p.ssm_norm_w + c0);
;       y[c][0] *= rstd * nw.x; y[c][1] *= rstd * nw.y; y[c][2] *= rstd * nw.z; y[c][3] *= rstd * nw.w;
;       am = fmaxf(am, fmaxf(fmaxf(fabsf(y[c][0]), fabsf(y[c][1])), fmaxf(fabsf(y[c][2]), fabsf(y[c][3]))));
;     }
;     am = wave_max_fast(am);
	v_mov_b32_e32 v60, v104
	v_mov_b32_e32 v61, v105
	v_mov_b32_e32 v62, v106
	v_mov_b32_e32 v63, v107
	v_mov_b32_e32 v64, v108
	v_mov_b32_e32 v65, v109
	v_mov_b32_e32 v66, v110
	v_mov_b32_e32 v67, v111
	v_pk_fma_f32 v[52:53], v[58:59], v[58:59], v[52:53]
	v_lshl_add_u64 v[68:69], v[34:35], 0, v[32:33]
	v_pk_fma_f32 v[52:53], v[48:49], v[48:49], v[52:53]
	v_mov_b32_e32 v72, v120
	v_mov_b32_e32 v73, v121
	v_mov_b32_e32 v76, v122
	v_mov_b32_e32 v77, v123
	v_mov_b32_e32 v78, v124
	v_mov_b32_e32 v79, v125
	v_mov_b32_e32 v70, v52
	v_mov_b32_e32 v54, v53
	v_pk_add_f32 v[52:53], v[70:71], v[54:55]
	s_nop 1
	v_mov_b32_dpp v55, v53 quad_perm:[1,0,3,2] row_mask:0xf bank_mask:0xf bound_ctrl:1
	v_mov_b32_dpp v54, v52 quad_perm:[1,0,3,2] row_mask:0xf bank_mask:0xf bound_ctrl:1
	v_pk_add_f32 v[52:53], v[52:53], v[54:55]
	s_nop 1
	v_mov_b32_dpp v55, v53 quad_perm:[2,3,0,1] row_mask:0xf bank_mask:0xf bound_ctrl:1
	v_mov_b32_dpp v54, v52 quad_perm:[2,3,0,1] row_mask:0xf bank_mask:0xf bound_ctrl:1
	v_pk_add_f32 v[52:53], v[52:53], v[54:55]
	s_nop 1
	v_mov_b32_dpp v55, v53 row_ror:4 row_mask:0xf bank_mask:0xf bound_ctrl:1
	v_mov_b32_dpp v54, v52 row_ror:4 row_mask:0xf bank_mask:0xf bound_ctrl:1
	v_pk_add_f32 v[70:71], v[52:53], v[54:55]
	v_mov_b32_e32 v52, v112
	v_mov_b32_e32 v53, v113
	v_mov_b32_e32 v54, v114
	v_mov_b32_e32 v55, v115
	s_nop 0
	v_mov_b32_dpp v81, v71 row_ror:8 row_mask:0xf bank_mask:0xf bound_ctrl:1
	v_mov_b32_dpp v80, v70 row_ror:8 row_mask:0xf bank_mask:0xf bound_ctrl:1
	v_pk_add_f32 v[70:71], v[70:71], v[80:81]
	ds_bpermute_b32 v81, v39, v71
	ds_bpermute_b32 v80, v39, v70
	s_waitcnt lgkmcnt(0)
	v_pk_add_f32 v[70:71], v[70:71], v[80:81]
	v_mov_b32_e32 v80, v126
	v_mov_b32_e32 v81, v127
	ds_bpermute_b32 v69, v74, v71
	ds_bpermute_b32 v68, v74, v70
	s_waitcnt lgkmcnt(0)
	v_pk_add_f32 v[82:83], v[70:71], v[68:69]
	v_mov_b32_e32 v68, v116
	v_mov_b32_e32 v69, v117
	v_mov_b32_e32 v70, v118
	v_mov_b32_e32 v71, v119
	v_pk_fma_f32 v[82:83], v[82:83], s[30:31], v[38:39] op_sel_hi:[1,0,0]
	s_waitcnt vmcnt(5)
	v_lshlrev_b32_e32 v85, 16, v73
	v_mul_f32_e32 v84, 0x4b800000, v83
	v_cmp_gt_f32_e32 vcc, s21, v83
	v_cmp_gt_f32_e64 s[12:13], s21, v82
	v_and_b32_e32 v73, 0xffff0000, v73
	v_cndmask_b32_e32 v83, v83, v84, vcc
	v_rsq_f32_e32 v83, v83
	v_mul_f32_e32 v84, 0x4b800000, v82
	v_cndmask_b32_e64 v82, v82, v84, s[12:13]
	v_rsq_f32_e32 v82, v82
	v_mul_f32_e32 v84, 0x45800000, v83
	v_cndmask_b32_e32 v83, v83, v84, vcc
	v_mul_f32_e32 v60, v60, v83
	v_mul_f32_e32 v60, v40, v60
	v_mul_f32_e32 v40, v83, v61
	v_mul_f32_e32 v61, v42, v40
	v_mul_f32_e32 v40, v83, v62
	v_mul_f32_e32 v44, v44, v40
	v_mul_f32_e32 v40, v83, v63
	v_mul_f32_e32 v64, v83, v64
	v_mul_f32_e32 v84, 0x45800000, v82
	v_max_f32_e64 v86, |v73|, |v73|
	v_max_f32_e64 v87, |v85|, |v85|
	v_mul_f32_e32 v46, v46, v40
	v_mul_f32_e32 v41, v41, v64
	v_mul_f32_e32 v64, v83, v65
	v_cndmask_b32_e64 v82, v82, v84, s[12:13]
	v_lshlrev_b32_e32 v84, 16, v72
	v_and_b32_e32 v72, 0xffff0000, v72
	v_max_f32_e32 v86, v87, v86
	v_max_f32_e64 v40, |v44|, |v46|
	v_mul_f32_e32 v64, v43, v64
	v_mul_f32_e32 v43, v83, v66
	v_max3_f32 v86, |v84|, |v72|, v86
	v_max3_f32 v40, |v60|, |v61|, v40
	s_waitcnt vmcnt(4)
	v_lshlrev_b32_e32 v62, 16, v76
	v_and_b32_e32 v63, 0xffff0000, v76
	v_lshlrev_b32_e32 v76, 16, v77
	v_and_b32_e32 v77, 0xffff0000, v77
	v_mul_f32_e32 v45, v45, v43
	v_mul_f32_e32 v43, v83, v67
	v_max3_f32 v40, v86, 0, v40
	v_max_f32_e64 v42, |v77|, |v77|
	v_max_f32_e64 v86, |v76|, |v76|
	v_mul_f32_e32 v47, v47, v43
	v_max_f32_e32 v42, v86, v42
	v_max_f32_e64 v43, |v45|, |v47|
	v_max3_f32 v42, |v62|, |v63|, v42
	v_max3_f32 v43, |v41|, |v64|, v43
	s_waitcnt vmcnt(3)
	v_lshlrev_b32_e32 v65, 16, v78
	v_and_b32_e32 v66, 0xffff0000, v78
	v_lshlrev_b32_e32 v67, 16, v79
	v_and_b32_e32 v78, 0xffff0000, v79
	v_max3_f32 v40, v40, v42, v43
	v_max_f32_e64 v42, |v78|, |v78|
	v_max_f32_e64 v43, |v67|, |v67|
	v_max_f32_e32 v42, v43, v42
	s_waitcnt vmcnt(2)
	v_mul_f32_e32 v43, v82, v52
	v_mul_f32_e32 v50, v50, v43
	v_mul_f32_e32 v43, v82, v53
	v_mul_f32_e32 v52, v56, v43
	v_mul_f32_e32 v43, v82, v54
	v_mul_f32_e32 v53, v58, v43
	v_mul_f32_e32 v43, v82, v55
	v_mul_f32_e32 v48, v48, v43
	v_max_f32_e64 v43, |v53|, |v48|
	v_max3_f32 v42, |v65|, |v66|, v42
	v_max3_f32 v43, |v50|, |v52|, v43
	s_waitcnt vmcnt(1)
	v_lshlrev_b32_e32 v56, 16, v81
	v_and_b32_e32 v58, 0xffff0000, v81
	v_max3_f32 v40, v40, v42, v43
	v_max_f32_e64 v42, |v58|, |v58|
	v_max_f32_e64 v43, |v56|, |v56|
	v_max_f32_e32 v42, v43, v42
	s_waitcnt vmcnt(0)
	v_mul_f32_e32 v43, v82, v68
	v_mul_f32_e32 v51, v51, v43
	v_mul_f32_e32 v43, v82, v69
	v_mul_f32_e32 v57, v57, v43
	v_mul_f32_e32 v43, v82, v70
	v_mul_f32_e32 v59, v59, v43
	v_mul_f32_e32 v43, v82, v71
	v_mul_f32_e32 v49, v49, v43
	v_lshlrev_b32_e32 v54, 16, v80
	v_and_b32_e32 v55, 0xffff0000, v80
	v_max_f32_e64 v43, |v59|, |v49|
	v_max3_f32 v42, |v54|, |v55|, v42
	v_max3_f32 v43, |v51|, |v57|, v43
	v_max3_f32 v40, v40, v42, v43
	s_nop 1
	v_mov_b32_dpp v42, v40 quad_perm:[1,0,3,2] row_mask:0xf bank_mask:0xf bound_ctrl:1
	v_max_f32_e32 v42, v42, v42
	v_max_f32_e32 v40, v40, v42
	s_nop 1
	v_mov_b32_dpp v42, v40 quad_perm:[2,3,0,1] row_mask:0xf bank_mask:0xf bound_ctrl:1
	v_max_f32_e32 v42, v42, v42
	v_max_f32_e32 v40, v40, v42
	s_nop 1
	v_mov_b32_dpp v42, v40 row_ror:4 row_mask:0xf bank_mask:0xf bound_ctrl:1
	v_max_f32_e32 v42, v42, v42
	v_max_f32_e32 v40, v40, v42
	s_nop 1
	v_mov_b32_dpp v42, v40 row_ror:8 row_mask:0xf bank_mask:0xf bound_ctrl:1
	v_max_f32_e32 v42, v42, v42
	v_max_f32_e32 v40, v40, v42
	ds_bpermute_b32 v42, v39, v40
	s_waitcnt lgkmcnt(0)
; __device__ __forceinline__ float bflo(uint32_t w) { return __uint_as_float(w << 16); }
; __device__ __forceinline__ float bfhi(uint32_t w) { return __uint_as_float(w & 0xffff0000u); }
; __device__ void phase_ssm_post(KParams& p, int bid, int nb, char* smem) {
;     ...
;     am = wave_max_fast(am);
;     const float inv = (am > 0.f) ? 127.f / am : 0.f;
; #pragma unroll
;     for (int c = 0; c < 4; ++c) {
;       const int c0 = c * 256 + lane * 4;
;       *reinterpret_cast<uint32_t*>(p.ycat8 + (size_t)t * D + c0) =
;           pack_i8x4(bflo(fq[c].x) * inv, bfhi(fq[c].x) * inv, bflo(fq[c].y) * inv, bfhi(fq[c].y) * inv);
;       *reinterpret_cast<uint32_t*>(p.ycat8 + (size_t)t * D + 1024 + c0) = pack_i8x4(y[c][0] * inv, y[c][1] * inv, y[c][2] * inv, y[c][3] * inv);
;     }
;     if (lane == 0) p.yscale[t] = am * (1.f / 127.f);
	v_max_f32_e32 v42, v42, v42
	v_max_f32_e32 v40, v40, v42
	ds_bpermute_b32 v42, v74, v40
	s_waitcnt lgkmcnt(0)
	v_max_f32_e32 v42, v42, v42
	v_max_f32_e32 v40, v40, v42
	v_div_scale_f32 v42, s[12:13], v40, v40, s31
	v_rcp_f32_e32 v43, v42
	s_nop 0
	v_fma_f32 v68, -v42, v43, 1.0
	v_fmac_f32_e32 v43, v68, v43
	v_div_scale_f32 v68, vcc, s31, v40, s31
	v_mul_f32_e32 v69, v68, v43
	v_fma_f32 v70, -v42, v69, v68
	v_fmac_f32_e32 v69, v70, v43
	v_fma_f32 v42, -v42, v69, v68
	v_div_fmas_f32 v42, v42, v43, v69
	v_div_fixup_f32 v42, v42, v40, s31
	v_cmp_lt_f32_e32 vcc, 0, v40
	s_nop 1
	v_cndmask_b32_e32 v68, 0, v42, vcc
	v_mul_f32_e32 v43, v68, v72
	v_mul_f32_e32 v61, v61, v68
	v_mul_f32_e32 v42, v68, v84
	v_mul_f32_e32 v69, v68, v85
	v_rndne_f32_e32 v43, v43
	v_mul_f32_e32 v60, v60, v68
	v_mul_f32_e32 v44, v44, v68
	v_mul_f32_e32 v46, v46, v68
	v_rndne_f32_e32 v61, v61
	v_mul_f32_e32 v70, v68, v73
	v_rndne_f32_e32 v42, v42
	v_cvt_i32_f32_e32 v43, v43
	v_rndne_f32_e32 v69, v69
	v_rndne_f32_e32 v60, v60
	v_cvt_i32_f32_e32 v61, v61
	v_rndne_f32_e32 v44, v44
	v_rndne_f32_e32 v46, v46
	v_cvt_i32_f32_e32 v42, v42
	v_cvt_i32_f32_sdwa v69, v69 dst_sel:WORD_1 dst_unused:UNUSED_PAD src0_sel:DWORD
	v_rndne_f32_e32 v70, v70
	v_cvt_i32_f32_e32 v60, v60
	v_cvt_i32_f32_sdwa v44, v44 dst_sel:WORD_1 dst_unused:UNUSED_PAD src0_sel:DWORD
	v_cvt_i32_f32_e32 v46, v46
	v_cvt_i32_f32_sdwa v70, v70 dst_sel:BYTE_3 dst_unused:UNUSED_PAD src0_sel:DWORD
	v_lshlrev_b32_e32 v43, 8, v43
	v_lshlrev_b32_e32 v61, 8, v61
	v_and_b32_e32 v69, 0xff0000, v69
	v_perm_b32 v42, v43, v42, s36
	v_and_b32_e32 v61, 0xff00, v61
	v_and_b32_e32 v44, 0xff0000, v44
	v_perm_b32 v46, v46, v60, s37
	v_or3_b32 v69, v42, v70, v69
	v_lshl_add_u64 v[42:43], v[26:27], 0, v[30:31]
	v_or3_b32 v44, v46, v61, v44
	v_mul_f32_e32 v46, v68, v63
	global_store_dword v[42:43], v44, off offset:1024
	v_mul_f32_e32 v44, v68, v62
	v_mul_f32_e32 v60, v68, v76
	v_rndne_f32_e32 v46, v46
	v_mul_f32_e32 v61, v68, v77
	v_rndne_f32_e32 v44, v44
	v_cvt_i32_f32_e32 v46, v46
	v_rndne_f32_e32 v60, v60
	v_cvt_i32_f32_e32 v44, v44
	v_cvt_i32_f32_sdwa v60, v60 dst_sel:WORD_1 dst_unused:UNUSED_PAD src0_sel:DWORD
	v_rndne_f32_e32 v61, v61
	v_cvt_i32_f32_sdwa v61, v61 dst_sel:BYTE_3 dst_unused:UNUSED_PAD src0_sel:DWORD
	v_lshlrev_b32_e32 v46, 8, v46
	v_and_b32_e32 v60, 0xff0000, v60
	v_perm_b32 v44, v46, v44, s36
	v_or3_b32 v44, v44, v61, v60
	global_store_dword v[42:43], v44, off offset:256
	v_mul_f32_e32 v44, v64, v68
	v_mul_f32_e32 v41, v41, v68
	v_mul_f32_e32 v45, v45, v68
	v_mul_f32_e32 v46, v47, v68
	v_rndne_f32_e32 v44, v44
	v_rndne_f32_e32 v41, v41
	v_cvt_i32_f32_e32 v44, v44
	v_rndne_f32_e32 v45, v45
	v_rndne_f32_e32 v46, v46
	v_cvt_i32_f32_e32 v41, v41
	v_cvt_i32_f32_sdwa v45, v45 dst_sel:WORD_1 dst_unused:UNUSED_PAD src0_sel:DWORD
	v_cvt_i32_f32_e32 v46, v46
	v_lshlrev_b32_e32 v44, 8, v44
	v_and_b32_e32 v44, 0xff00, v44
	v_and_b32_e32 v45, 0xff0000, v45
	v_perm_b32 v41, v46, v41, s37
	v_or3_b32 v41, v41, v44, v45
	v_mul_f32_e32 v44, v68, v66
	global_store_dword v[42:43], v41, off offset:1280
	v_mul_f32_e32 v41, v68, v65
	v_mul_f32_e32 v45, v68, v67
	v_rndne_f32_e32 v44, v44
	v_mul_f32_e32 v46, v68, v78
	v_rndne_f32_e32 v41, v41
	v_cvt_i32_f32_e32 v44, v44
	v_rndne_f32_e32 v45, v45
	v_cvt_i32_f32_e32 v41, v41
	v_cvt_i32_f32_sdwa v45, v45 dst_sel:WORD_1 dst_unused:UNUSED_PAD src0_sel:DWORD
	v_rndne_f32_e32 v46, v46
	v_cvt_i32_f32_sdwa v46, v46 dst_sel:BYTE_3 dst_unused:UNUSED_PAD src0_sel:DWORD
	v_lshlrev_b32_e32 v44, 8, v44
	v_and_b32_e32 v45, 0xff0000, v45
	v_perm_b32 v41, v44, v41, s36
	v_or3_b32 v41, v41, v46, v45
	v_mul_f32_e32 v44, v52, v68
	global_store_dword v[42:43], v41, off offset:512
	v_mul_f32_e32 v41, v50, v68
	v_mul_f32_e32 v45, v53, v68
	v_mul_f32_e32 v46, v48, v68
	v_rndne_f32_e32 v44, v44
	v_rndne_f32_e32 v41, v41
	v_cvt_i32_f32_e32 v44, v44
	v_rndne_f32_e32 v45, v45
	v_rndne_f32_e32 v46, v46
	v_cvt_i32_f32_e32 v41, v41
	v_cvt_i32_f32_sdwa v45, v45 dst_sel:WORD_1 dst_unused:UNUSED_PAD src0_sel:DWORD
	v_cvt_i32_f32_e32 v46, v46
	v_lshlrev_b32_e32 v44, 8, v44
	v_and_b32_e32 v44, 0xff00, v44
	v_and_b32_e32 v45, 0xff0000, v45
	v_perm_b32 v41, v46, v41, s37
	v_or3_b32 v41, v41, v44, v45
	v_mul_f32_e32 v44, v68, v55
	global_store_dword v[42:43], v41, off offset:1536
	v_mul_f32_e32 v41, v68, v54
	v_mul_f32_e32 v45, v68, v56
	v_rndne_f32_e32 v44, v44
	v_mul_f32_e32 v46, v68, v58
	v_rndne_f32_e32 v41, v41
	v_cvt_i32_f32_e32 v44, v44
	v_rndne_f32_e32 v45, v45
	v_cvt_i32_f32_e32 v41, v41
	v_cvt_i32_f32_sdwa v45, v45 dst_sel:WORD_1 dst_unused:UNUSED_PAD src0_sel:DWORD
	v_rndne_f32_e32 v46, v46
	v_cvt_i32_f32_sdwa v46, v46 dst_sel:BYTE_3 dst_unused:UNUSED_PAD src0_sel:DWORD
	v_lshlrev_b32_e32 v44, 8, v44
	v_and_b32_e32 v45, 0xff0000, v45
	v_perm_b32 v41, v44, v41, s36
	v_or3_b32 v41, v41, v46, v45
	v_mul_f32_e32 v44, v57, v68
	global_store_dword v[42:43], v41, off offset:768
	v_mul_f32_e32 v41, v51, v68
	v_mul_f32_e32 v45, v59, v68
	v_mul_f32_e32 v46, v49, v68
	v_rndne_f32_e32 v44, v44
	v_rndne_f32_e32 v41, v41
	v_cvt_i32_f32_e32 v44, v44
	v_rndne_f32_e32 v45, v45
	v_rndne_f32_e32 v46, v46
	v_cvt_i32_f32_e32 v41, v41
	v_cvt_i32_f32_sdwa v45, v45 dst_sel:WORD_1 dst_unused:UNUSED_PAD src0_sel:DWORD
	v_cvt_i32_f32_e32 v46, v46
	v_lshlrev_b32_e32 v44, 8, v44
	v_and_b32_e32 v44, 0xff00, v44
	v_and_b32_e32 v45, 0xff0000, v45
	v_perm_b32 v41, v46, v41, s37
	v_or3_b32 v41, v41, v44, v45
	global_store_dword v[42:43], v69, off
	global_store_dword v[42:43], v41, off offset:1792
	s_and_saveexec_b64 s[12:13], s[8:9]
	s_cbranch_execz .LBB0_1002
	v_mul_f32_e32 v40, 0x3c010204, v40
	global_store_dword v[28:29], v40, off
	s_branch .LBB0_1002
